# MoBA selected-block sub-tiles: running max folded into the score initialisation (no per-score subtract); rescale adjusts scores in the rare path
# speedup vs baseline: 1.0157x; 1.0055x over previous
; __device__ __forceinline__ float max2_raw(float a, float b) { float d; asm("v_max_f32 %0, %1, %2" : "=v"(d) : "v"(a), "v"(b)); return d; }
; template <int MODE>
; __device__ __forceinline__ void attn_moba_sub(const bf16x8 (&qr)[4], f32x16& O0, f32x16& O1, float& m, float& l, unsigned saddr, int j, int kv0, int q, int q0, int hi, float slope2, bool rowok) {
;     bf16x8 kf[4], vf[2][2];
;     asm volatile("ds_read_b128 %0, %8\n\tds_read_b128 %1, %8 offset:1024\n\tds_read_b128 %2, %8 offset:2048\n\tds_read_b128 %3, %8 offset:3072\n\t"
;                  "ds_read_b128 %4, %9\n\tds_read_b128 %5, %9 offset:1024\n\tds_read_b128 %6, %9 offset:2048\n\tds_read_b128 %7, %9 offset:3072\n\ts_waitcnt lgkmcnt(0)"
;                  : "=&v"(kf[0]), "=&v"(kf[1]), "=&v"(kf[2]), "=&v"(kf[3]), "=&v"(vf[0][0]), "=&v"(vf[0][1]), "=&v"(vf[1][0]), "=&v"(vf[1][1])
;                  : "v"(saddr + (unsigned)j * 4096u), "v"(saddr + 8192u + (unsigned)j * 4096u) : "memory");
;     f32x16 S; const float sbase = slope2 * (float)(kv0 + 8 * hi - q0);
; #pragma unroll
;     for (int r = 0; r < 16; ++r) S[r] = sbase + slope2 * (float)((r & 7) + 16 * (r >> 3));
; #pragma unroll
;     for (int d0 = 0; d0 < 4; ++d0) S = __builtin_amdgcn_mfma_f32_32x32x16_bf16(kf[d0], qr[d0], S, 0, 0, 0);
;     if (MODE == 1) {
; #pragma unroll
;         for (int r = 0; r < 16; ++r) { const int key = kv0 + (r & 7) + 8 * hi + 16 * (r >> 3); if (key > q) S[r] = -INFINITY; }
;     }
;     if (MODE == 2) { if (!rowok) {
; #pragma unroll
;         for (int r = 0; r < 16; ++r) S[r] = -INFINITY; } }
;     float rm = rowmax16_raw(S);
;     { const auto rr = __builtin_amdgcn_permlane32_swap(__float_as_uint(rm), __float_as_uint(rm), false, false); rm = max2_raw(__uint_as_float(rr[0]), __uint_as_float(rr[1])); }
;     if (__any(rm > m)) { const float mn = fmaxf(fmaxf(m, rm), -1e30f); const float alpha = __builtin_amdgcn_exp2f(m - mn); l *= alpha; O0 *= alpha; O1 *= alpha; m = mn; }
.LBB0_1331:
	s_lshr_b32 s0, s92, 2
	s_lshl_b32 s0, 1, s0
	s_and_b32 s1, s0, s79
	s_cmp_eq_u32 s1, 0
	s_cbranch_scc1 .LBB0_1337
	v_add_u32_e32 v113, s89, v195
	s_nop 1
	v_add_u32_e32 v80, 0xe0, v113
	v_add_u32_e32 v229, 0x1000, v198
	v_add_u32_e32 v230, 0x3000, v198
	v_cvt_f32_i32_e32 v80, v80
	ds_read_b128 v[114:117], v229
	ds_read_b128 v[118:121], v229 offset:1024
	ds_read_b128 v[122:125], v229 offset:2048
	ds_read_b128 v[144:147], v229 offset:3072
	ds_read_b128 v[108:111], v230
	ds_read_b128 v[100:103], v230 offset:1024
	ds_read_b128 v[104:107], v230 offset:2048
	ds_read_b128 v[96:99], v230 offset:3072
	v_add_u32_e32 v228, 0x2000, v198
	v_and_b32_e32 v112, s0, v193
	v_cmp_eq_u32_e64 s[70:71], 0, v112
	v_fma_f32 v80, v163, v80, -v196
	s_nop 0
	v_cndmask_b32_e64 v80, v80, v190, s[70:71]
	v_pk_add_f32 v[94:95], v[176:177], v[80:81] op_sel_hi:[1,0]
	v_pk_add_f32 v[92:93], v[174:175], v[80:81] op_sel_hi:[1,0]
	v_pk_add_f32 v[90:91], v[172:173], v[80:81] op_sel_hi:[1,0]
	v_pk_add_f32 v[88:89], v[170:171], v[80:81] op_sel_hi:[1,0]
	v_pk_add_f32 v[86:87], v[168:169], v[80:81] op_sel_hi:[1,0]
	v_pk_add_f32 v[84:85], v[166:167], v[80:81] op_sel_hi:[1,0]
	v_pk_add_f32 v[82:83], v[164:165], v[80:81] op_sel_hi:[1,0]
	v_pk_add_f32 v[80:81], v[162:163], v[80:81] op_sel_hi:[1,0]
	s_waitcnt lgkmcnt(4)
	s_nop 1
	v_mfma_f32_32x32x16_bf16 v[80:95], v[114:117], v[128:131], v[80:95]
	v_mfma_f32_32x32x16_bf16 v[80:95], v[118:121], v[132:135], v[80:95]
	v_mfma_f32_32x32x16_bf16 v[80:95], v[122:125], v[136:139], v[80:95]
	v_mfma_f32_32x32x16_bf16 v[80:95], v[144:147], v[140:143], v[80:95]
	ds_read_b128 v[114:117], v198
	ds_read_b128 v[118:121], v198 offset:1024
	ds_read_b128 v[122:125], v198 offset:2048
	ds_read_b128 v[144:147], v198 offset:3072
	s_nop 7
	v_max3_f32 v222, v80, v81, v82
	v_max3_f32 v223, v83, v84, v85
	v_max3_f32 v224, v86, v87, v88
	v_max3_f32 v222, v222, v223, v224
	v_max3_f32 v223, v89, v90, v91
	v_max3_f32 v224, v92, v93, v94
	v_max3_f32 v223, v223, v224, v95
	v_max_f32_e32 v222, v222, v223
	v_mov_b32_e32 v223, v222
	s_nop 1
	v_permlane32_swap_b32_e32 v222, v223
	v_max_f32_e32 v223, v222, v223
	v_cmp_lt_f32_e32 vcc, 0, v223
	s_cbranch_vccz .Lmoba_m2_1
	v_add_f32_e32 v223, v223, v196
	v_max3_f32 v227, v196, v223, s86
	v_sub_f32_e32 v226, v196, v227
	v_add_f32_e32 v80, v80, v226
	v_add_f32_e32 v81, v81, v226
	v_add_f32_e32 v82, v82, v226
	v_add_f32_e32 v83, v83, v226
	v_add_f32_e32 v84, v84, v226
	v_add_f32_e32 v85, v85, v226
	v_add_f32_e32 v86, v86, v226
	v_add_f32_e32 v87, v87, v226
	v_add_f32_e32 v88, v88, v226
	v_add_f32_e32 v89, v89, v226
	v_add_f32_e32 v90, v90, v226
	v_add_f32_e32 v91, v91, v226
	v_add_f32_e32 v92, v92, v226
	v_add_f32_e32 v93, v93, v226
	v_add_f32_e32 v94, v94, v226
	v_add_f32_e32 v95, v95, v226
	v_exp_f32_e32 v226, v226
	v_mov_b32_e32 v196, v227
	v_mul_f32_e32 v197, v197, v226
	v_pk_mul_f32 v[62:63], v[62:63], v[226:227] op_sel_hi:[1,0]
	v_pk_mul_f32 v[60:61], v[60:61], v[226:227] op_sel_hi:[1,0]
	v_pk_mul_f32 v[58:59], v[58:59], v[226:227] op_sel_hi:[1,0]
	v_pk_mul_f32 v[56:57], v[56:57], v[226:227] op_sel_hi:[1,0]
	v_pk_mul_f32 v[54:55], v[54:55], v[226:227] op_sel_hi:[1,0]
	v_pk_mul_f32 v[52:53], v[52:53], v[226:227] op_sel_hi:[1,0]
	v_pk_mul_f32 v[50:51], v[50:51], v[226:227] op_sel_hi:[1,0]
	v_pk_mul_f32 v[48:49], v[48:49], v[226:227] op_sel_hi:[1,0]
	v_pk_mul_f32 v[78:79], v[78:79], v[226:227] op_sel_hi:[1,0]
	v_pk_mul_f32 v[76:77], v[76:77], v[226:227] op_sel_hi:[1,0]
	v_pk_mul_f32 v[74:75], v[74:75], v[226:227] op_sel_hi:[1,0]
	v_pk_mul_f32 v[72:73], v[72:73], v[226:227] op_sel_hi:[1,0]
	v_pk_mul_f32 v[70:71], v[70:71], v[226:227] op_sel_hi:[1,0]
	v_pk_mul_f32 v[68:69], v[68:69], v[226:227] op_sel_hi:[1,0]
	v_pk_mul_f32 v[66:67], v[66:67], v[226:227] op_sel_hi:[1,0]
	v_pk_mul_f32 v[64:65], v[64:65], v[226:227] op_sel_hi:[1,0]
; __device__ __forceinline__ unsigned pk2(float lo, float hi) { const f32x2_pk v = {lo, hi}; return __builtin_bit_cast(unsigned, __builtin_convertvector(v, bf16x2)); }
; __device__ __forceinline__ float max2_raw(float a, float b) { float d; asm("v_max_f32 %0, %1, %2" : "=v"(d) : "v"(a), "v"(b)); return d; }
; template <int MODE>
; __device__ __forceinline__ void attn_moba_sub(const bf16x8 (&qr)[4], f32x16& O0, f32x16& O1, float& m, float& l, unsigned saddr, int j, int kv0, int q, int q0, int hi, float slope2, bool rowok) {
;     ...
;     f32x16 S; const float sbase = slope2 * (float)(kv0 + 8 * hi - q0);
; #pragma unroll
;     for (int r = 0; r < 16; ++r) S[r] = sbase + slope2 * (float)((r & 7) + 16 * (r >> 3));
; #pragma unroll
;     for (int d0 = 0; d0 < 4; ++d0) S = __builtin_amdgcn_mfma_f32_32x32x16_bf16(kf[d0], qr[d0], S, 0, 0, 0);
;     if (MODE == 1) {
; #pragma unroll
;         for (int r = 0; r < 16; ++r) { const int key = kv0 + (r & 7) + 8 * hi + 16 * (r >> 3); if (key > q) S[r] = -INFINITY; }
;     }
;     if (MODE == 2) { if (!rowok) {
; #pragma unroll
;         for (int r = 0; r < 16; ++r) S[r] = -INFINITY; } }
;     float rm = rowmax16_raw(S);
;     { const auto rr = __builtin_amdgcn_permlane32_swap(__float_as_uint(rm), __float_as_uint(rm), false, false); rm = max2_raw(__uint_as_float(rr[0]), __uint_as_float(rr[1])); }
;     if (__any(rm > m)) { const float mn = fmaxf(fmaxf(m, rm), -1e30f); const float alpha = __builtin_amdgcn_exp2f(m - mn); l *= alpha; O0 *= alpha; O1 *= alpha; m = mn; }
;     float p[16]; float ps = 0.f;
; #pragma unroll
;     for (int r = 0; r < 16; ++r) { p[r] = __builtin_amdgcn_exp2f(S[r] - m); ps += p[r]; }
;     l += ps;
;     u32x4 w0, w1;
;     w0.x = pk2(p[0], p[1]); w0.y = pk2(p[2], p[3]); w0.z = pk2(p[4], p[5]); w0.w = pk2(p[6], p[7]);
;     w1.x = pk2(p[8], p[9]); w1.y = pk2(p[10], p[11]); w1.z = pk2(p[12], p[13]); w1.w = pk2(p[14], p[15]);
;     const bf16x8 pf0 = __builtin_bit_cast(bf16x8, w0), pf1 = __builtin_bit_cast(bf16x8, w1);
;     O0 = __builtin_amdgcn_mfma_f32_32x32x16_bf16(vf[0][0], pf0, O0, 0, 0, 0); O0 = __builtin_amdgcn_mfma_f32_32x32x16_bf16(vf[1][0], pf1, O0, 0, 0, 0);
;     O1 = __builtin_amdgcn_mfma_f32_32x32x16_bf16(vf[0][1], pf0, O1, 0, 0, 0); O1 = __builtin_amdgcn_mfma_f32_32x32x16_bf16(vf[1][1], pf1, O1, 0, 0, 0);
.Lmoba_m2_1:
	v_exp_f32_e32 v80, v80
	v_exp_f32_e32 v81, v81
	v_exp_f32_e32 v82, v82
	v_exp_f32_e32 v83, v83
	v_add_f32_e32 v225, 0, v80
	v_exp_f32_e32 v84, v84
	v_add_f32_e32 v225, v81, v225
	v_exp_f32_e32 v85, v85
	v_add_f32_e32 v225, v82, v225
	v_exp_f32_e32 v86, v86
	v_add_f32_e32 v225, v83, v225
	v_exp_f32_e32 v87, v87
	v_add_f32_e32 v225, v84, v225
	v_exp_f32_e32 v88, v88
	v_add_f32_e32 v225, v85, v225
	v_exp_f32_e32 v89, v89
	v_add_f32_e32 v225, v86, v225
	v_exp_f32_e32 v90, v90
	v_add_f32_e32 v225, v87, v225
	v_exp_f32_e32 v91, v91
	v_cvt_pk_bf16_f32 v80, v80, v81
	v_cvt_pk_bf16_f32 v81, v82, v83
	v_cvt_pk_bf16_f32 v82, v84, v85
	v_cvt_pk_bf16_f32 v83, v86, v87
	v_add_f32_e32 v225, v88, v225
	v_exp_f32_e32 v92, v92
	s_waitcnt lgkmcnt(4)
	v_mfma_f32_32x32x16_bf16 v[48:63], v[108:111], v[80:83], v[48:63]
	v_add_f32_e32 v225, v89, v225
	v_exp_f32_e32 v93, v93
	v_add_f32_e32 v225, v90, v225
	v_exp_f32_e32 v94, v94
	v_add_f32_e32 v225, v91, v225
	v_exp_f32_e32 v95, v95
	v_mfma_f32_32x32x16_bf16 v[64:79], v[100:103], v[80:83], v[64:79]
	v_add_f32_e32 v225, v92, v225
	v_add_f32_e32 v225, v93, v225
	v_add_f32_e32 v225, v94, v225
	v_add_f32_e32 v225, v95, v225
	v_cvt_pk_bf16_f32 v84, v88, v89
	v_cvt_pk_bf16_f32 v85, v90, v91
	v_cvt_pk_bf16_f32 v86, v92, v93
	v_cvt_pk_bf16_f32 v87, v94, v95
	v_add_f32_e32 v112, v197, v225
	s_nop 0
	v_mfma_f32_32x32x16_bf16 v[48:63], v[104:107], v[84:87], v[48:63]
	v_mfma_f32_32x32x16_bf16 v[64:79], v[96:99], v[84:87], v[64:79]
	ds_read_b128 v[108:111], v228
	ds_read_b128 v[100:103], v228 offset:1024
	ds_read_b128 v[104:107], v228 offset:2048
	ds_read_b128 v[96:99], v228 offset:3072
	v_add_u32_e32 v80, 0xc0, v113
	v_cvt_f32_i32_e32 v80, v80
	v_fma_f32 v80, v163, v80, -v196
	v_cndmask_b32_e64 v80, v80, v190, s[70:71]
	v_pk_add_f32 v[94:95], v[176:177], v[80:81] op_sel_hi:[1,0]
	v_pk_add_f32 v[92:93], v[174:175], v[80:81] op_sel_hi:[1,0]
	v_pk_add_f32 v[90:91], v[172:173], v[80:81] op_sel_hi:[1,0]
	v_pk_add_f32 v[88:89], v[170:171], v[80:81] op_sel_hi:[1,0]
	v_pk_add_f32 v[86:87], v[168:169], v[80:81] op_sel_hi:[1,0]
	v_pk_add_f32 v[84:85], v[166:167], v[80:81] op_sel_hi:[1,0]
	v_pk_add_f32 v[82:83], v[164:165], v[80:81] op_sel_hi:[1,0]
	v_pk_add_f32 v[80:81], v[162:163], v[80:81] op_sel_hi:[1,0]
	s_waitcnt lgkmcnt(4)
	s_nop 1
	v_mfma_f32_32x32x16_bf16 v[80:95], v[114:117], v[128:131], v[80:95]
	v_mfma_f32_32x32x16_bf16 v[80:95], v[118:121], v[132:135], v[80:95]
	v_mfma_f32_32x32x16_bf16 v[80:95], v[122:125], v[136:139], v[80:95]
	v_mfma_f32_32x32x16_bf16 v[80:95], v[144:147], v[140:143], v[80:95]
	s_nop 11
	v_max3_f32 v222, v80, v81, v82
	v_max3_f32 v223, v83, v84, v85
	v_max3_f32 v224, v86, v87, v88
	v_max3_f32 v222, v222, v223, v224
	v_max3_f32 v223, v89, v90, v91
	v_max3_f32 v224, v92, v93, v94
	v_max3_f32 v223, v223, v224, v95
	v_max_f32_e32 v222, v222, v223
	v_mov_b32_e32 v223, v222
	s_nop 1
	v_permlane32_swap_b32_e32 v222, v223
	v_max_f32_e32 v223, v222, v223
	v_cmp_lt_f32_e32 vcc, 0, v223
	s_cbranch_vccz .Lmoba_m2_2
	v_add_f32_e32 v223, v223, v196
	v_max3_f32 v227, v196, v223, s86
	v_sub_f32_e32 v226, v196, v227
	v_add_f32_e32 v80, v80, v226
	v_add_f32_e32 v81, v81, v226
	v_add_f32_e32 v82, v82, v226
	v_add_f32_e32 v83, v83, v226
	v_add_f32_e32 v84, v84, v226
	v_add_f32_e32 v85, v85, v226
	v_add_f32_e32 v86, v86, v226
	v_add_f32_e32 v87, v87, v226
	v_add_f32_e32 v88, v88, v226
	v_add_f32_e32 v89, v89, v226
	v_add_f32_e32 v90, v90, v226
	v_add_f32_e32 v91, v91, v226
	v_add_f32_e32 v92, v92, v226
	v_add_f32_e32 v93, v93, v226
	v_add_f32_e32 v94, v94, v226
	v_add_f32_e32 v95, v95, v226
	v_exp_f32_e32 v226, v226
	v_mov_b32_e32 v196, v227
	v_mul_f32_e32 v112, v226, v112
	v_pk_mul_f32 v[62:63], v[62:63], v[226:227] op_sel_hi:[1,0]
	v_pk_mul_f32 v[60:61], v[60:61], v[226:227] op_sel_hi:[1,0]
	v_pk_mul_f32 v[58:59], v[58:59], v[226:227] op_sel_hi:[1,0]
	v_pk_mul_f32 v[56:57], v[56:57], v[226:227] op_sel_hi:[1,0]
	v_pk_mul_f32 v[54:55], v[54:55], v[226:227] op_sel_hi:[1,0]
	v_pk_mul_f32 v[52:53], v[52:53], v[226:227] op_sel_hi:[1,0]
	v_pk_mul_f32 v[50:51], v[50:51], v[226:227] op_sel_hi:[1,0]
	v_pk_mul_f32 v[48:49], v[48:49], v[226:227] op_sel_hi:[1,0]
	v_pk_mul_f32 v[78:79], v[78:79], v[226:227] op_sel_hi:[1,0]
	v_pk_mul_f32 v[76:77], v[76:77], v[226:227] op_sel_hi:[1,0]
	v_pk_mul_f32 v[74:75], v[74:75], v[226:227] op_sel_hi:[1,0]
	v_pk_mul_f32 v[72:73], v[72:73], v[226:227] op_sel_hi:[1,0]
	v_pk_mul_f32 v[70:71], v[70:71], v[226:227] op_sel_hi:[1,0]
	v_pk_mul_f32 v[68:69], v[68:69], v[226:227] op_sel_hi:[1,0]
	v_pk_mul_f32 v[66:67], v[66:67], v[226:227] op_sel_hi:[1,0]
	v_pk_mul_f32 v[64:65], v[64:65], v[226:227] op_sel_hi:[1,0]
.Lmoba_m2_2:
	v_exp_f32_e32 v80, v80
	v_exp_f32_e32 v81, v81
	v_exp_f32_e32 v82, v82
	v_exp_f32_e32 v83, v83
	v_add_f32_e32 v225, 0, v80
	v_exp_f32_e32 v84, v84
	v_add_f32_e32 v225, v81, v225
	v_exp_f32_e32 v85, v85
	v_add_f32_e32 v225, v82, v225
	v_exp_f32_e32 v86, v86
	v_add_f32_e32 v225, v83, v225
	v_exp_f32_e32 v87, v87
	v_add_f32_e32 v225, v84, v225
	v_exp_f32_e32 v88, v88
	v_add_f32_e32 v225, v85, v225
	v_exp_f32_e32 v89, v89
	v_add_f32_e32 v225, v86, v225
	v_exp_f32_e32 v90, v90
	v_add_f32_e32 v225, v87, v225
	v_exp_f32_e32 v91, v91
	v_cvt_pk_bf16_f32 v80, v80, v81
	v_cvt_pk_bf16_f32 v81, v82, v83
	v_cvt_pk_bf16_f32 v82, v84, v85
	v_cvt_pk_bf16_f32 v83, v86, v87
	v_add_f32_e32 v225, v88, v225
	v_exp_f32_e32 v92, v92
	s_waitcnt lgkmcnt(0)
	v_mfma_f32_32x32x16_bf16 v[48:63], v[108:111], v[80:83], v[48:63]
	v_add_f32_e32 v225, v89, v225
	v_exp_f32_e32 v93, v93
	v_add_f32_e32 v225, v90, v225
	v_exp_f32_e32 v94, v94
	v_add_f32_e32 v225, v91, v225
	v_exp_f32_e32 v95, v95
	v_mfma_f32_32x32x16_bf16 v[64:79], v[100:103], v[80:83], v[64:79]
	v_add_f32_e32 v225, v92, v225
	v_add_f32_e32 v225, v93, v225
	v_add_f32_e32 v225, v94, v225
	v_add_f32_e32 v225, v95, v225
	v_cvt_pk_bf16_f32 v84, v88, v89
	v_cvt_pk_bf16_f32 v85, v90, v91
	v_cvt_pk_bf16_f32 v86, v92, v93
	v_cvt_pk_bf16_f32 v87, v94, v95
	v_add_f32_e32 v197, v112, v225
	s_nop 0
	v_mfma_f32_32x32x16_bf16 v[48:63], v[104:107], v[84:87], v[48:63]
	v_mfma_f32_32x32x16_bf16 v[64:79], v[96:99], v[84:87], v[64:79]
